# attention loop: K/V tiles fetched two tiles ahead into two register sets; staging writes lead the MFMA segment; loop head 64-byte aligned
# speedup vs baseline: 1.0344x; 1.0140x over previous
; #define AT_LOADK(t) do { const int kr_ = AT_KROW(t); _Pragma("unroll") for (int i_ = 0; i_ < 2; ++i_) kreg[i_] = *(const u32x4*)(Kp + (size_t)(kr_ + prow0 + 32 * i_) * 512 + pch * 8); } while (0)
; #define AT_LOADV(t) do { const int kr_ = AT_KROW(t); _Pragma("unroll") for (int i_ = 0; i_ < 2; ++i_) vreg[i_] = *(const u32x4*)(Vp + (size_t)(kr_ + prow0 + 32 * i_) * 512 + pch * 8); } while (0)
; #define AT_STOREK(st) do { _Pragma("unroll") for (int i_ = 0; i_ < 2; ++i_) *(LAS u32x4*)(L + AT_K + (st) * AT_KBYTES + (prow0 + 32 * i_) * AT_KSTR + pch * 16) = kreg[i_]; } while (0)
; #define AT_STOREV(st) do { _Pragma("unroll") for (int i_ = 0; i_ < 2; ++i_) *(LAS u32x4*)(L + AT_V + (st) * AT_VBYTES + (prow0 + 32 * i_) * AT_VSTR + pch * 16) = vreg[i_]; } while (0)
; __device__ __forceinline__ void attn_unit(const Frame& F, int layer, int qrow0, int ntiles, int b, int head, float lam, float m2, float lam_init) {
;     ...
;     if (wave >= 4) __builtin_amdgcn_s_setprio(1);
;     AT_LOADK(0); AT_LOADV(0); AT_STOREK(0); AT_STOREV(0);
;     if (ntiles > 1) { AT_LOADK(1); AT_STOREK(1); }
;     __syncthreads();
.LBB0_549:
	s_add_u32 s42, s4, s30
	s_addc_u32 s43, s5, 0
	s_add_u32 s2, s2, s30
	s_addc_u32 s3, s3, 0
	s_lshl_b32 s4, s16, 8
	v_ashrrev_i32_e32 v186, 4, v32
	s_add_i32 s5, s4, 0x8000
	s_add_i32 s16, s4, 0x8040
	v_lshlrev_b32_e32 v3, 4, v32
	v_add_u32_e32 v128, s5, v186
	v_and_b32_e32 v144, 0xf0, v3
	v_add_u32_e32 v20, s16, v186
	v_lshl_add_u64 v[4:5], s[2:3], 0, v[144:145]
	s_mov_b64 s[2:3], 0x31534800
	v_ashrrev_i32_e32 v129, 31, v128
	v_ashrrev_i32_e32 v21, 31, v20
	v_lshl_add_u64 v[180:181], v[4:5], 0, s[2:3]
	v_lshlrev_b64 v[12:13], 10, v[128:129]
	s_mov_b64 s[2:3], 0x8000
	v_lshl_add_u64 v[16:17], s[42:43], 0, v[144:145]
	s_mov_b64 s[42:43], 0x33934800
	v_lshlrev_b64 v[62:63], 10, v[20:21]
	v_lshl_add_u64 v[14:15], v[12:13], 0, s[2:3]
	v_lshl_add_u64 v[182:183], v[16:17], 0, s[42:43]
	v_lshl_add_u64 v[96:97], v[62:63], 0, s[2:3]
	v_lshl_add_u64 v[4:5], v[180:181], 0, v[12:13]
	v_lshl_add_u64 v[8:9], v[180:181], 0, v[14:15]
	v_lshl_add_u64 v[12:13], v[182:183], 0, v[12:13]
	v_lshl_add_u64 v[16:17], v[182:183], 0, v[14:15]
	v_lshl_add_u64 v[20:21], v[180:181], 0, v[62:63]
	v_lshl_add_u64 v[24:25], v[180:181], 0, v[96:97]
	global_load_dwordx4 v[4:7], v[4:5], off
	s_nop 0
	global_load_dwordx4 v[8:11], v[8:9], off
	s_nop 0
	global_load_dwordx4 v[12:15], v[12:13], off
	s_nop 0
	global_load_dwordx4 v[16:19], v[16:17], off
	s_nop 0
	global_load_dwordx4 v[20:23], v[20:21], off
	s_nop 0
	global_load_dwordx4 v[24:27], v[24:25], off
	v_or_b32_e32 v1, s15, v1
	s_movk_i32 s16, 0x140
	v_mul_u32_u24_e32 v0, 0x110, v0
	v_mul_lo_u32 v198, v186, s24
	v_mul_lo_u32 v199, v186, s16
	v_lshlrev_b32_e32 v1, 1, v1
	v_add_u32_e32 v200, 0, v144
	v_xor_b32_e32 v64, 0x80000000, v2
	v_add_u32_e32 v2, 0x2800, v199
	v_add3_u32 v197, 0, v0, v1
	v_add_u32_e32 v144, v200, v198
	v_add_u32_e32 v194, v200, v199
	v_add_u32_e32 v195, v200, v2
	v_mov_b32_e32 v65, v64
	v_mov_b32_e32 v66, v64
	v_mov_b32_e32 v67, v64
	v_mov_b32_e32 v68, v64
	v_mov_b32_e32 v69, v64
	v_mov_b32_e32 v70, v64
	v_mov_b32_e32 v71, v64
	v_mov_b32_e32 v72, v64
	v_mov_b32_e32 v73, v64
	v_mov_b32_e32 v74, v64
	v_mov_b32_e32 v75, v64
	v_mov_b32_e32 v76, v64
	v_mov_b32_e32 v77, v64
	v_mov_b32_e32 v78, v64
	v_mov_b32_e32 v79, v64
	v_and_b32_e32 v193, 63, v32
	v_and_b32_e32 v33, 16, v32
	s_mov_b32 s15, 0x8000
	s_mov_b32 s2, 4
	s_mov_b32 s3, 0
	s_add_i32 s5, s4, 0x8080
	s_add_i32 s4, s4, 0x80c0
	s_waitcnt vmcnt(5)
	ds_write_b128 v144, v[4:7]
	s_waitcnt vmcnt(4)
	ds_write_b128 v144, v[8:11] offset:8704
	s_waitcnt vmcnt(3)
	ds_write_b128 v194, v[12:15] offset:34816
	s_waitcnt vmcnt(2)
	ds_write_b128 v195, v[16:19] offset:34816
	s_waitcnt vmcnt(1)
	ds_write_b128 v144, v[20:23] offset:17408
	s_waitcnt vmcnt(0)
	ds_write_b128 v144, v[24:27] offset:26112
	s_waitcnt lgkmcnt(0)
	s_barrier
	v_readfirstlane_b32 s72, v180
	v_readfirstlane_b32 s73, v181
	v_readfirstlane_b32 s74, v182
	v_readfirstlane_b32 s75, v183
	v_lshl_add_u32 v178, v186, 10, v200
	v_mov_b32_e32 v252, v64
	s_add_i32 s42, s4, 0xffffff40
	s_add_i32 s43, s4, 0xffff7f40
	s_lshl_b32 s43, s43, 3
	s_add_i32 s43, s43, 0xffffff00
	s_mov_b32 s2, 0
	s_add_i32 s5, s2, 2
	s_cmp_ge_u32 s5, 36
	s_cbranch_scc1 .Latt_nokload_pro1
	s_cmp_lt_u32 s5, 4
	s_cselect_b32 s15, s42, s43
	s_lshl_b32 s45, s5, 6
	s_add_i32 s15, s15, s45
	s_lshl_b32 s15, s15, 10
	v_add_u32_e32 v186, s15, v178
	v_add_u32_e32 v187, 0x8000, v186
	global_load_dwordx4 v[162:165], v186, s[72:73]
	global_load_dwordx4 v[166:169], v187, s[72:73]
.Latt_nokload_pro1:
	s_add_i32 s5, s2, 1
	s_cmp_ge_u32 s5, 36
	s_cbranch_scc1 .Latt_novload_pro1
	s_cmp_lt_u32 s5, 4
	s_cselect_b32 s15, s42, s43
	s_lshl_b32 s45, s5, 6
	s_add_i32 s15, s15, s45
	s_lshl_b32 s15, s15, 10
	v_add_u32_e32 v188, s15, v178
	v_add_u32_e32 v189, 0x8000, v188
	global_load_dwordx4 v[170:173], v188, s[74:75]
	global_load_dwordx4 v[174:177], v189, s[74:75]
; __device__ __forceinline__ unsigned pk2(float lo, float hi) { f32x2_t v = {lo, hi}; bf16x2_t b = __builtin_convertvector(v, bf16x2_t); return __builtin_bit_cast(unsigned, b); }
; __device__ __forceinline__ void lds_barrier() { asm volatile("s_waitcnt lgkmcnt(0)" ::: "memory"); __builtin_amdgcn_s_barrier(); asm volatile("" ::: "memory"); }
; #define AT_LOADK(t) do { const int kr_ = AT_KROW(t); _Pragma("unroll") for (int i_ = 0; i_ < 2; ++i_) kreg[i_] = *(const u32x4*)(Kp + (size_t)(kr_ + prow0 + 32 * i_) * 512 + pch * 8); } while (0)
; #define AT_LOADV(t) do { const int kr_ = AT_KROW(t); _Pragma("unroll") for (int i_ = 0; i_ < 2; ++i_) vreg[i_] = *(const u32x4*)(Vp + (size_t)(kr_ + prow0 + 32 * i_) * 512 + pch * 8); } while (0)
; #define AT_STOREK(st) do { _Pragma("unroll") for (int i_ = 0; i_ < 2; ++i_) *(LAS u32x4*)(L + AT_K + (st) * AT_KBYTES + (prow0 + 32 * i_) * AT_KSTR + pch * 16) = kreg[i_]; } while (0)
; #define AT_STOREV(st) do { _Pragma("unroll") for (int i_ = 0; i_ < 2; ++i_) *(LAS u32x4*)(L + AT_V + (st) * AT_VBYTES + (prow0 + 32 * i_) * AT_VSTR + pch * 16) = vreg[i_]; } while (0)
; __device__ __forceinline__ void attn_unit(const Frame& F, int layer, int qrow0, int ntiles, int b, int head, float lam, float m2, float lam_init) {
;     ...
;     AT_LOADK(0); AT_LOADV(0); AT_STOREK(0); AT_STOREV(0);
;     if (ntiles > 1) { AT_LOADK(1); AT_STOREK(1); }
;     __syncthreads();
;     f32x16 sa, sb, na, nb;
;     AT_QK(sa, sb, 0);
;     lds_barrier();
;     for (int t = 0; t < ntiles; ++t) {
;         if (t + 2 < ntiles) AT_LOADK(t + 2);
;         if (t + 1 < ntiles) AT_LOADV(t + 1);
;         if (t + 1 < ntiles) AT_QK(na, nb, (t + 1) & 1);
;         float ls = 0.f;
; #pragma unroll
;         for (int i = 0; i < 16; ++i) { sa[i] = __builtin_amdgcn_exp2f(sa[i]); sb[i] = __builtin_amdgcn_exp2f(sb[i]); ls += sa[i] + sb[i]; }
;         lsum += ls;
;         bf16x8 pk[4];
;         { u32x4 w0, w1, w2, w3;
; #pragma unroll
;           for (int i = 0; i < 4; ++i) { w0[i] = pk2(sa[2 * i], sa[2 * i + 1]); w1[i] = pk2(sa[8 + 2 * i], sa[9 + 2 * i]); w2[i] = pk2(sb[2 * i], sb[2 * i + 1]); w3[i] = pk2(sb[8 + 2 * i], sb[9 + 2 * i]); }
;           pk[0] = __builtin_bit_cast(bf16x8, w0); pk[1] = __builtin_bit_cast(bf16x8, w1); pk[2] = __builtin_bit_cast(bf16x8, w2); pk[3] = __builtin_bit_cast(bf16x8, w3); }
.Latt_novload_pro1:
	v_bfe_u32 v186, v193, 2, 2
	v_lshrrev_b32_e32 v187, 5, v193
	v_lshl_add_u32 v186, v187, 2, v186
	v_mul_u32_u24_e32 v196, 0x140, v186
	v_bfe_u32 v187, v193, 4, 1
	v_and_b32_e32 v188, 3, v193
	v_lshl_add_u32 v196, v188, 3, v196
	v_lshl_add_u32 v196, v187, 5, v196
	v_mov_b32_e32 v0, 0
	v_mov_b32_e32 v1, 0
	v_mov_b32_e32 v2, 0
	v_mov_b32_e32 v3, 0
	v_mov_b32_e32 v4, 0
	v_mov_b32_e32 v5, 0
	v_mov_b32_e32 v6, 0
	v_mov_b32_e32 v7, 0
	v_mov_b32_e32 v8, 0
	v_mov_b32_e32 v9, 0
	v_mov_b32_e32 v10, 0
	v_mov_b32_e32 v11, 0
	v_mov_b32_e32 v12, 0
	v_mov_b32_e32 v13, 0
	v_mov_b32_e32 v14, 0
	v_mov_b32_e32 v15, 0
	v_mov_b32_e32 v16, 0
	v_mov_b32_e32 v17, 0
	v_mov_b32_e32 v18, 0
	v_mov_b32_e32 v19, 0
	v_mov_b32_e32 v20, 0
	v_mov_b32_e32 v21, 0
	v_mov_b32_e32 v22, 0
	v_mov_b32_e32 v23, 0
	v_mov_b32_e32 v24, 0
	v_mov_b32_e32 v25, 0
	v_mov_b32_e32 v26, 0
	v_mov_b32_e32 v27, 0
	v_mov_b32_e32 v28, 0
	v_mov_b32_e32 v29, 0
	v_mov_b32_e32 v30, 0
	v_mov_b32_e32 v31, 0
	v_mov_b32_e32 v32, 0
	v_mov_b32_e32 v33, 0
	v_mov_b32_e32 v34, 0
	v_mov_b32_e32 v35, 0
	v_mov_b32_e32 v36, 0
	v_mov_b32_e32 v37, 0
	v_mov_b32_e32 v38, 0
	v_mov_b32_e32 v39, 0
	v_mov_b32_e32 v40, 0
	v_mov_b32_e32 v41, 0
	v_mov_b32_e32 v42, 0
	v_mov_b32_e32 v43, 0
	v_mov_b32_e32 v44, 0
	v_mov_b32_e32 v45, 0
	v_mov_b32_e32 v46, 0
	v_mov_b32_e32 v47, 0
	v_mov_b32_e32 v48, 0
	v_mov_b32_e32 v49, 0
	v_mov_b32_e32 v50, 0
	v_mov_b32_e32 v51, 0
	v_mov_b32_e32 v52, 0
	v_mov_b32_e32 v53, 0
	v_mov_b32_e32 v54, 0
	v_mov_b32_e32 v55, 0
	v_mov_b32_e32 v56, 0
	v_mov_b32_e32 v57, 0
	v_mov_b32_e32 v58, 0
	v_mov_b32_e32 v59, 0
	v_mov_b32_e32 v60, 0
	v_mov_b32_e32 v61, 0
	v_mov_b32_e32 v62, 0
	v_mov_b32_e32 v63, 0
	v_mov_b32_e32 v201, 0
	v_mov_b32_e32 v180, 0
	v_mov_b32_e32 v181, 0
	v_mov_b32_e32 v182, 0
	v_mov_b32_e32 v183, 0
	v_mov_b32_e32 v218, 0
	v_mov_b32_e32 v219, 0
	v_mov_b32_e32 v220, 0
	v_mov_b32_e32 v221, 0
	v_mov_b32_e32 v222, 0
	v_mov_b32_e32 v223, 0
	v_mov_b32_e32 v224, 0
	v_mov_b32_e32 v225, 0
	v_mov_b32_e32 v226, 0
	v_mov_b32_e32 v227, 0
	v_mov_b32_e32 v228, 0
	v_mov_b32_e32 v229, 0
	v_mov_b32_e32 v230, 0
	v_mov_b32_e32 v231, 0
	v_mov_b32_e32 v232, 0
	v_mov_b32_e32 v233, 0
	ds_read_b128 v[128:131], v197 offset:0
	ds_read_b128 v[132:135], v197 offset:8704
	ds_read_b128 v[136:139], v197 offset:32
	ds_read_b128 v[140:143], v197 offset:8736
	s_waitcnt lgkmcnt(2)
	v_mfma_f32_32x32x16_bf16 v[80:95], v[128:131], v[158:161], v[64:79]
	v_mfma_f32_32x32x16_bf16 v[96:111], v[132:135], v[158:161], v[64:79]
	ds_read_b128 v[128:131], v197 offset:64
	ds_read_b128 v[132:135], v197 offset:8768
	s_waitcnt lgkmcnt(2)
	v_mfma_f32_32x32x16_bf16 v[80:95], v[136:139], v[154:157], v[80:95]
	v_mfma_f32_32x32x16_bf16 v[96:111], v[140:143], v[154:157], v[96:111]
	ds_read_b128 v[136:139], v197 offset:96
	ds_read_b128 v[140:143], v197 offset:8800
	s_waitcnt lgkmcnt(2)
	v_mfma_f32_32x32x16_bf16 v[80:95], v[128:131], v[150:153], v[80:95]
	v_mfma_f32_32x32x16_bf16 v[96:111], v[132:135], v[150:153], v[96:111]
	s_waitcnt lgkmcnt(0)
	v_mfma_f32_32x32x16_bf16 v[80:95], v[136:139], v[146:149], v[80:95]
	v_mfma_f32_32x32x16_bf16 v[96:111], v[140:143], v[146:149], v[96:111]
	s_cmp_lt_u32 s12, 4
	s_cbranch_scc1 .Latt_lead0
	s_barrier
.Latt_lead0:
	s_nop 7
	s_nop 7
	.p2align 6
.Latt_loop:
	s_add_i32 s5, s2, 3
	s_cmp_ge_u32 s5, 36
	s_cbranch_scc1 .Latt_nokload_it0
	s_cmp_lt_u32 s5, 4
	s_cselect_b32 s15, s42, s43
	s_lshl_b32 s45, s5, 6
	s_add_i32 s15, s15, s45
	s_lshl_b32 s15, s15, 10
	v_add_u32_e32 v186, s15, v178
	v_add_u32_e32 v187, 0x8000, v186
	global_load_dwordx4 v[234:237], v186, s[72:73]
	global_load_dwordx4 v[238:241], v187, s[72:73]
.Latt_nokload_it0:
	s_add_i32 s5, s2, 2
	s_cmp_ge_u32 s5, 36
	s_cbranch_scc1 .Latt_novload_it0
	s_cmp_lt_u32 s5, 4
	s_cselect_b32 s15, s42, s43
	s_lshl_b32 s45, s5, 6
	s_add_i32 s15, s15, s45
	s_lshl_b32 s15, s15, 10
	v_add_u32_e32 v188, s15, v178
	v_add_u32_e32 v189, 0x8000, v188
	global_load_dwordx4 v[242:245], v188, s[74:75]
	global_load_dwordx4 v[248:251], v189, s[74:75]
.Latt_novload_it0:
	v_exp_f32_e32 v80, v80
	v_exp_f32_e32 v96, v96
	v_exp_f32_e32 v81, v81
	v_exp_f32_e32 v97, v97
	v_exp_f32_e32 v82, v82
	v_exp_f32_e32 v98, v98
	v_exp_f32_e32 v83, v83
	v_exp_f32_e32 v99, v99
	v_exp_f32_e32 v84, v84
	v_exp_f32_e32 v100, v100
	v_exp_f32_e32 v85, v85
	v_exp_f32_e32 v101, v101
	v_exp_f32_e32 v86, v86
	v_exp_f32_e32 v102, v102
	v_exp_f32_e32 v87, v87
	v_exp_f32_e32 v103, v103
	v_exp_f32_e32 v88, v88
	v_exp_f32_e32 v104, v104
	v_exp_f32_e32 v89, v89
	v_exp_f32_e32 v105, v105
	v_exp_f32_e32 v90, v90
	v_exp_f32_e32 v106, v106
	v_exp_f32_e32 v91, v91
	v_exp_f32_e32 v107, v107
	v_exp_f32_e32 v92, v92
	v_exp_f32_e32 v108, v108
	v_exp_f32_e32 v93, v93
	v_exp_f32_e32 v109, v109
	v_exp_f32_e32 v94, v94
	v_exp_f32_e32 v110, v110
	v_exp_f32_e32 v95, v95
	v_exp_f32_e32 v111, v111
	v_cvt_pk_bf16_f32 v112, v80, v81
	v_cvt_pk_bf16_f32 v113, v82, v83
	v_cvt_pk_bf16_f32 v114, v84, v85
	v_cvt_pk_bf16_f32 v115, v86, v87
	v_cvt_pk_bf16_f32 v116, v88, v89
	v_cvt_pk_bf16_f32 v117, v90, v91
	v_cvt_pk_bf16_f32 v118, v92, v93
	v_cvt_pk_bf16_f32 v119, v94, v95
	v_cvt_pk_bf16_f32 v120, v96, v97
	v_cvt_pk_bf16_f32 v121, v98, v99
	v_cvt_pk_bf16_f32 v122, v100, v101
	v_cvt_pk_bf16_f32 v123, v102, v103
	v_cvt_pk_bf16_f32 v124, v104, v105
	v_cvt_pk_bf16_f32 v125, v106, v107
	v_cvt_pk_bf16_f32 v126, v108, v109
	v_cvt_pk_bf16_f32 v127, v110, v111
	v_add_f32_e32 v80, v80, v96
	v_add_f32_e32 v81, v81, v97
	v_add_f32_e32 v82, v82, v98
	v_add_f32_e32 v83, v83, v99
	v_add_f32_e32 v84, v84, v100
	v_add_f32_e32 v85, v85, v101
	v_add_f32_e32 v86, v86, v102
	v_add_f32_e32 v87, v87, v103
	v_add_f32_e32 v88, v88, v104
	v_add_f32_e32 v89, v89, v105
	v_add_f32_e32 v90, v90, v106
	v_add_f32_e32 v91, v91, v107
	v_add_f32_e32 v92, v92, v108
	v_add_f32_e32 v93, v93, v109
	v_add_f32_e32 v94, v94, v110
	v_add_f32_e32 v95, v95, v111
	v_add_f32_e32 v80, v80, v88
	v_add_f32_e32 v81, v81, v89
	v_add_f32_e32 v82, v82, v90
	v_add_f32_e32 v83, v83, v91
	v_add_f32_e32 v84, v84, v92
	v_add_f32_e32 v85, v85, v93
	v_add_f32_e32 v86, v86, v94
	v_add_f32_e32 v87, v87, v95
	v_add_f32_e32 v80, v80, v84
	v_add_f32_e32 v81, v81, v85
	v_add_f32_e32 v82, v82, v86
	v_add_f32_e32 v83, v83, v87
	v_add_f32_e32 v80, v80, v82
	v_add_f32_e32 v81, v81, v83
	v_add_f32_e32 v80, v80, v81
	v_add_f32_e32 v201, v201, v80
	s_add_i32 s5, s2, 0
	s_and_b32 s5, s5, 1
	s_mul_i32 s15, s5, 0x5000
	v_add_u32_e32 v191, s15, v196
	s_mul_i32 s15, s5, 0x4400
	s_add_i32 s16, s2, 2
	s_cmp_ge_u32 s16, 36
	s_cselect_b32 s15, 80000, s15
	v_add_u32_e32 v179, s15, v144
	s_xor_b32 s5, s5, 1
	s_mul_i32 s15, s5, 0x4400
	v_add_u32_e32 v190, s15, v197
	s_mul_i32 s15, s5, 0x5000
	s_add_i32 s16, s2, 1
	s_cmp_ge_u32 s16, 36
	s_cselect_b32 s15, 62592, s15
	v_add_u32_e32 v185, s15, v194
	s_barrier
	s_add_i32 s5, s2, 3
	s_cmp_ge_u32 s5, 36
	s_cbranch_scc1 .Latt_drain_0
	s_waitcnt vmcnt(4)
	s_branch .Latt_stage_0

; #define LAS __attribute__((address_space(3)))
; __device__ __forceinline__ unsigned pk2(float lo, float hi) { f32x2_t v = {lo, hi}; bf16x2_t b = __builtin_convertvector(v, bf16x2_t); return __builtin_bit_cast(unsigned, b); }
; #define MFMA32(a, b, c) __builtin_amdgcn_mfma_f32_32x32x16_bf16((a), (b), (c), 0, 0, 0)
; __device__ __forceinline__ void attn_unit(const Frame& F, int layer, int qrow0, int ntiles, int b, int head, float lam, float m2, float lam_init) {
;     ...
;         if (t + 1 < ntiles) AT_QK(na, nb, (t + 1) & 1);
;         float ls = 0.f;
; #pragma unroll
;         for (int i = 0; i < 16; ++i) { sa[i] = __builtin_amdgcn_exp2f(sa[i]); sb[i] = __builtin_amdgcn_exp2f(sb[i]); ls += sa[i] + sb[i]; }
;         lsum += ls;
;         bf16x8 pk[4];
;         { u32x4 w0, w1, w2, w3;
; #pragma unroll
;           for (int i = 0; i < 4; ++i) { w0[i] = pk2(sa[2 * i], sa[2 * i + 1]); w1[i] = pk2(sa[8 + 2 * i], sa[9 + 2 * i]); w2[i] = pk2(sb[2 * i], sb[2 * i + 1]); w3[i] = pk2(sb[8 + 2 * i], sb[9 + 2 * i]); }
;           pk[0] = __builtin_bit_cast(bf16x8, w0); pk[1] = __builtin_bit_cast(bf16x8, w1); pk[2] = __builtin_bit_cast(bf16x8, w2); pk[3] = __builtin_bit_cast(bf16x8, w3); }
;         LAS const unsigned char* Vt = L + AT_V + (t & 1) * AT_VBYTES;
;         __builtin_amdgcn_sched_barrier(0);
;         bf16x8 vfa[4], vfb[4];
; #pragma unroll
;         for (int j = 0; j < 4; ++j) vfa[j] = frag_tr_acc(Vt, AT_VSTR, 0, 32 * j, lane);
; #pragma unroll
;         for (int ks = 0; ks < 4; ks += 2) {
; #pragma unroll
;             for (int j = 0; j < 4; ++j) vfb[j] = frag_tr_acc(Vt, AT_VSTR, 16 * (ks + 1), 32 * j, lane);
; #pragma unroll
;             for (int j = 0; j < 4; ++j) o[j] = MFMA32(pk[ks], vfa[j], o[j]);
;             __builtin_amdgcn_sched_barrier(0);
;             if (ks + 2 < 4) {
; #pragma unroll
;                 for (int j = 0; j < 4; ++j) vfa[j] = frag_tr_acc(Vt, AT_VSTR, 16 * (ks + 2), 32 * j, lane);
;             }
; #pragma unroll
;             for (int j = 0; j < 4; ++j) o[j] = MFMA32(pk[ks + 1], vfb[j], o[j]);
;             __builtin_amdgcn_sched_barrier(0);
;         }
;         if (t + 2 < ntiles) AT_STOREK(t & 1);
;         if (t + 1 < ntiles) AT_STOREV((t + 1) & 1);
.Latt_stage_0:
	ds_write_b128 v179, v[162:165]
	ds_write_b128 v179, v[166:169] offset:8704
	ds_write_b128 v185, v[170:173] offset:34816
	ds_write_b128 v185, v[174:177] offset:45056
	s_add_i32 s5, s2, 1
	s_cmp_ge_u32 s5, 36
	s_cbranch_scc1 .Latt_noqk_0
	ds_read_b128 v[128:131], v190 offset:0
	ds_read_b128 v[132:135], v190 offset:8704
	ds_read_b128 v[136:139], v190 offset:32
	ds_read_b128 v[140:143], v190 offset:8736
	ds_read_b64_tr_b16 v[202:203], v191 offset:34816
	ds_read_b64_tr_b16 v[206:207], v191 offset:34880
	ds_read_b64_tr_b16 v[210:211], v191 offset:34944
	ds_read_b64_tr_b16 v[214:215], v191 offset:35008
	s_waitcnt lgkmcnt(6)
	v_mfma_f32_32x32x16_bf16 v[80:95], v[128:131], v[158:161], v[64:79]
	v_mfma_f32_32x32x16_bf16 v[96:111], v[132:135], v[158:161], v[64:79]
	ds_read_b128 v[128:131], v190 offset:64
	ds_read_b128 v[132:135], v190 offset:8768
	ds_read_b64_tr_b16 v[204:205], v191 offset:37376
	ds_read_b64_tr_b16 v[208:209], v191 offset:37440
	ds_read_b64_tr_b16 v[212:213], v191 offset:37504
	ds_read_b64_tr_b16 v[216:217], v191 offset:37568
	s_waitcnt lgkmcnt(10)
	v_mfma_f32_32x32x16_bf16 v[80:95], v[136:139], v[154:157], v[80:95]
	v_mfma_f32_32x32x16_bf16 v[96:111], v[140:143], v[154:157], v[96:111]
	ds_read_b128 v[136:139], v190 offset:96
	ds_read_b128 v[140:143], v190 offset:8800
	s_waitcnt lgkmcnt(6)
	v_mfma_f32_32x32x16_bf16 v[80:95], v[128:131], v[150:153], v[80:95]
	v_mfma_f32_32x32x16_bf16 v[96:111], v[132:135], v[150:153], v[96:111]
	ds_read_b64_tr_b16 v[218:219], v191 offset:39936
	ds_read_b64_tr_b16 v[222:223], v191 offset:40000
	ds_read_b64_tr_b16 v[226:227], v191 offset:40064
	ds_read_b64_tr_b16 v[230:231], v191 offset:40128
	ds_read_b64_tr_b16 v[220:221], v191 offset:42496
	ds_read_b64_tr_b16 v[224:225], v191 offset:42560
	ds_read_b64_tr_b16 v[228:229], v191 offset:42624
	ds_read_b64_tr_b16 v[232:233], v191 offset:42688
	s_waitcnt lgkmcnt(8)
	v_mfma_f32_32x32x16_bf16 v[80:95], v[136:139], v[146:149], v[80:95]
	v_mfma_f32_32x32x16_bf16 v[96:111], v[140:143], v[146:149], v[96:111]
	s_branch .Latt_pv_0
.Latt_noqk_0:
	ds_read_b64_tr_b16 v[202:203], v191 offset:34816
	ds_read_b64_tr_b16 v[206:207], v191 offset:34880
	ds_read_b64_tr_b16 v[210:211], v191 offset:34944
	ds_read_b64_tr_b16 v[214:215], v191 offset:35008
	ds_read_b64_tr_b16 v[204:205], v191 offset:37376
	ds_read_b64_tr_b16 v[208:209], v191 offset:37440
	ds_read_b64_tr_b16 v[212:213], v191 offset:37504
	ds_read_b64_tr_b16 v[216:217], v191 offset:37568
	ds_read_b64_tr_b16 v[218:219], v191 offset:39936
	ds_read_b64_tr_b16 v[222:223], v191 offset:40000
	ds_read_b64_tr_b16 v[226:227], v191 offset:40064
	s_waitcnt lgkmcnt(14)
	ds_read_b64_tr_b16 v[230:231], v191 offset:40128
	s_waitcnt lgkmcnt(14)
	ds_read_b64_tr_b16 v[220:221], v191 offset:42496
	s_waitcnt lgkmcnt(14)
	ds_read_b64_tr_b16 v[224:225], v191 offset:42560
	s_waitcnt lgkmcnt(14)
	ds_read_b64_tr_b16 v[228:229], v191 offset:42624
	s_waitcnt lgkmcnt(14)
	ds_read_b64_tr_b16 v[232:233], v191 offset:42688
	s_waitcnt lgkmcnt(8)
.Latt_pv_0:
	v_mfma_f32_32x32x16_bf16 v[32:47], v[112:115], v[202:205], v[32:47]
	v_mfma_f32_32x32x16_bf16 v[48:63], v[112:115], v[206:209], v[48:63]
	v_mfma_f32_32x32x16_bf16 v[0:15], v[112:115], v[210:213], v[0:15]
	v_mfma_f32_32x32x16_bf16 v[16:31], v[112:115], v[214:217], v[16:31]
	ds_read_b64_tr_b16 v[202:203], v191 offset:45056
	ds_read_b64_tr_b16 v[206:207], v191 offset:45120
	ds_read_b64_tr_b16 v[210:211], v191 offset:45184
	ds_read_b64_tr_b16 v[214:215], v191 offset:45248
	ds_read_b64_tr_b16 v[204:205], v191 offset:47616
	ds_read_b64_tr_b16 v[208:209], v191 offset:47680
	ds_read_b64_tr_b16 v[212:213], v191 offset:47744
	s_waitcnt lgkmcnt(14)
	ds_read_b64_tr_b16 v[216:217], v191 offset:47808
	s_waitcnt lgkmcnt(8)
	v_mfma_f32_32x32x16_bf16 v[32:47], v[116:119], v[218:221], v[32:47]
	v_mfma_f32_32x32x16_bf16 v[48:63], v[116:119], v[222:225], v[48:63]
	v_mfma_f32_32x32x16_bf16 v[0:15], v[116:119], v[226:229], v[0:15]
	v_mfma_f32_32x32x16_bf16 v[16:31], v[116:119], v[230:233], v[16:31]
	ds_read_b64_tr_b16 v[218:219], v191 offset:50176
	ds_read_b64_tr_b16 v[222:223], v191 offset:50240
	ds_read_b64_tr_b16 v[226:227], v191 offset:50304
	ds_read_b64_tr_b16 v[230:231], v191 offset:50368
	ds_read_b64_tr_b16 v[220:221], v191 offset:52736
	ds_read_b64_tr_b16 v[224:225], v191 offset:52800
	ds_read_b64_tr_b16 v[228:229], v191 offset:52864
	s_waitcnt lgkmcnt(14)
	ds_read_b64_tr_b16 v[232:233], v191 offset:52928
	s_waitcnt lgkmcnt(8)
	v_mfma_f32_32x32x16_bf16 v[32:47], v[120:123], v[202:205], v[32:47]
	v_mfma_f32_32x32x16_bf16 v[48:63], v[120:123], v[206:209], v[48:63]
	v_mfma_f32_32x32x16_bf16 v[0:15], v[120:123], v[210:213], v[0:15]
	v_mfma_f32_32x32x16_bf16 v[16:31], v[120:123], v[214:217], v[16:31]
	s_waitcnt lgkmcnt(0)
	v_mfma_f32_32x32x16_bf16 v[32:47], v[124:127], v[218:221], v[32:47]
	v_mfma_f32_32x32x16_bf16 v[48:63], v[124:127], v[222:225], v[48:63]
	v_mfma_f32_32x32x16_bf16 v[0:15], v[124:127], v[226:229], v[0:15]
	v_mfma_f32_32x32x16_bf16 v[16:31], v[124:127], v[230:233], v[16:31]
	s_barrier
	s_add_i32 s5, s2, 4
	s_cmp_ge_u32 s5, 36
	s_cbranch_scc1 .Latt_nokload_it1
	s_cmp_lt_u32 s5, 4
	s_cselect_b32 s15, s42, s43
	s_lshl_b32 s45, s5, 6
	s_add_i32 s15, s15, s45
	s_lshl_b32 s15, s15, 10
	v_add_u32_e32 v186, s15, v178
	v_add_u32_e32 v187, 0x8000, v186
	global_load_dwordx4 v[162:165], v186, s[72:73]
	global_load_dwordx4 v[166:169], v187, s[72:73]
; __device__ __forceinline__ unsigned pk2(float lo, float hi) { f32x2_t v = {lo, hi}; bf16x2_t b = __builtin_convertvector(v, bf16x2_t); return __builtin_bit_cast(unsigned, b); }
; #define AT_LOADK(t) do { const int kr_ = AT_KROW(t); _Pragma("unroll") for (int i_ = 0; i_ < 2; ++i_) kreg[i_] = *(const u32x4*)(Kp + (size_t)(kr_ + prow0 + 32 * i_) * 512 + pch * 8); } while (0)
; #define AT_LOADV(t) do { const int kr_ = AT_KROW(t); _Pragma("unroll") for (int i_ = 0; i_ < 2; ++i_) vreg[i_] = *(const u32x4*)(Vp + (size_t)(kr_ + prow0 + 32 * i_) * 512 + pch * 8); } while (0)
; __device__ __forceinline__ void attn_unit(const Frame& F, int layer, int qrow0, int ntiles, int b, int head, float lam, float m2, float lam_init) {
;     ...
;         if (t + 2 < ntiles) AT_LOADK(t + 2);
;         if (t + 1 < ntiles) AT_LOADV(t + 1);
;         if (t + 1 < ntiles) AT_QK(na, nb, (t + 1) & 1);
;         float ls = 0.f;
; #pragma unroll
;         for (int i = 0; i < 16; ++i) { sa[i] = __builtin_amdgcn_exp2f(sa[i]); sb[i] = __builtin_amdgcn_exp2f(sb[i]); ls += sa[i] + sb[i]; }
;         lsum += ls;
;         bf16x8 pk[4];
;         { u32x4 w0, w1, w2, w3;
; #pragma unroll
;           for (int i = 0; i < 4; ++i) { w0[i] = pk2(sa[2 * i], sa[2 * i + 1]); w1[i] = pk2(sa[8 + 2 * i], sa[9 + 2 * i]); w2[i] = pk2(sb[2 * i], sb[2 * i + 1]); w3[i] = pk2(sb[8 + 2 * i], sb[9 + 2 * i]); }
;           pk[0] = __builtin_bit_cast(bf16x8, w0); pk[1] = __builtin_bit_cast(bf16x8, w1); pk[2] = __builtin_bit_cast(bf16x8, w2); pk[3] = __builtin_bit_cast(bf16x8, w3); }
.Latt_nokload_it1:
	s_add_i32 s5, s2, 3
	s_cmp_ge_u32 s5, 36
	s_cbranch_scc1 .Latt_novload_it1
	s_cmp_lt_u32 s5, 4
	s_cselect_b32 s15, s42, s43
	s_lshl_b32 s45, s5, 6
	s_add_i32 s15, s15, s45
	s_lshl_b32 s15, s15, 10
	v_add_u32_e32 v188, s15, v178
	v_add_u32_e32 v189, 0x8000, v188
	global_load_dwordx4 v[170:173], v188, s[74:75]
	global_load_dwordx4 v[174:177], v189, s[74:75]
.Latt_novload_it1:
	v_exp_f32_e32 v80, v80
	v_exp_f32_e32 v96, v96
	v_exp_f32_e32 v81, v81
	v_exp_f32_e32 v97, v97
	v_exp_f32_e32 v82, v82
	v_exp_f32_e32 v98, v98
	v_exp_f32_e32 v83, v83
	v_exp_f32_e32 v99, v99
	v_exp_f32_e32 v84, v84
	v_exp_f32_e32 v100, v100
	v_exp_f32_e32 v85, v85
	v_exp_f32_e32 v101, v101
	v_exp_f32_e32 v86, v86
	v_exp_f32_e32 v102, v102
	v_exp_f32_e32 v87, v87
	v_exp_f32_e32 v103, v103
	v_exp_f32_e32 v88, v88
	v_exp_f32_e32 v104, v104
	v_exp_f32_e32 v89, v89
	v_exp_f32_e32 v105, v105
	v_exp_f32_e32 v90, v90
	v_exp_f32_e32 v106, v106
	v_exp_f32_e32 v91, v91
	v_exp_f32_e32 v107, v107
	v_exp_f32_e32 v92, v92
	v_exp_f32_e32 v108, v108
	v_exp_f32_e32 v93, v93
	v_exp_f32_e32 v109, v109
	v_exp_f32_e32 v94, v94
	v_exp_f32_e32 v110, v110
	v_exp_f32_e32 v95, v95
	v_exp_f32_e32 v111, v111
	v_cvt_pk_bf16_f32 v112, v80, v81
	v_cvt_pk_bf16_f32 v113, v82, v83
	v_cvt_pk_bf16_f32 v114, v84, v85
	v_cvt_pk_bf16_f32 v115, v86, v87
	v_cvt_pk_bf16_f32 v116, v88, v89
	v_cvt_pk_bf16_f32 v117, v90, v91
	v_cvt_pk_bf16_f32 v118, v92, v93
	v_cvt_pk_bf16_f32 v119, v94, v95
	v_cvt_pk_bf16_f32 v120, v96, v97
	v_cvt_pk_bf16_f32 v121, v98, v99
	v_cvt_pk_bf16_f32 v122, v100, v101
	v_cvt_pk_bf16_f32 v123, v102, v103
	v_cvt_pk_bf16_f32 v124, v104, v105
	v_cvt_pk_bf16_f32 v125, v106, v107
	v_cvt_pk_bf16_f32 v126, v108, v109
	v_cvt_pk_bf16_f32 v127, v110, v111
	v_add_f32_e32 v80, v80, v96
	v_add_f32_e32 v81, v81, v97
	v_add_f32_e32 v82, v82, v98
	v_add_f32_e32 v83, v83, v99
	v_add_f32_e32 v84, v84, v100
	v_add_f32_e32 v85, v85, v101
	v_add_f32_e32 v86, v86, v102
	v_add_f32_e32 v87, v87, v103
	v_add_f32_e32 v88, v88, v104
	v_add_f32_e32 v89, v89, v105
	v_add_f32_e32 v90, v90, v106
	v_add_f32_e32 v91, v91, v107
	v_add_f32_e32 v92, v92, v108
	v_add_f32_e32 v93, v93, v109
	v_add_f32_e32 v94, v94, v110
	v_add_f32_e32 v95, v95, v111
	v_add_f32_e32 v80, v80, v88
	v_add_f32_e32 v81, v81, v89
	v_add_f32_e32 v82, v82, v90
	v_add_f32_e32 v83, v83, v91
	v_add_f32_e32 v84, v84, v92
	v_add_f32_e32 v85, v85, v93
	v_add_f32_e32 v86, v86, v94
	v_add_f32_e32 v87, v87, v95
	v_add_f32_e32 v80, v80, v84
	v_add_f32_e32 v81, v81, v85
	v_add_f32_e32 v82, v82, v86
	v_add_f32_e32 v83, v83, v87
	v_add_f32_e32 v80, v80, v82
	v_add_f32_e32 v81, v81, v83
	v_add_f32_e32 v80, v80, v81
	v_add_f32_e32 v201, v201, v80
	s_add_i32 s5, s2, 1
	s_and_b32 s5, s5, 1
	s_mul_i32 s15, s5, 0x5000
	v_add_u32_e32 v191, s15, v196
	s_mul_i32 s15, s5, 0x4400
	s_add_i32 s16, s2, 3
	s_cmp_ge_u32 s16, 36
	s_cselect_b32 s15, 80000, s15
	v_add_u32_e32 v179, s15, v144
	s_xor_b32 s5, s5, 1
	s_mul_i32 s15, s5, 0x4400
	v_add_u32_e32 v190, s15, v197
	s_mul_i32 s15, s5, 0x5000
	s_add_i32 s16, s2, 2
	s_cmp_ge_u32 s16, 36
	s_cselect_b32 s15, 62592, s15
	v_add_u32_e32 v185, s15, v194
	s_barrier
	s_add_i32 s5, s2, 4
	s_cmp_ge_u32 s5, 36
	s_cbranch_scc1 .Latt_drain_1
	s_waitcnt vmcnt(4)
	s_branch .Latt_stage_1

; #define LAS __attribute__((address_space(3)))
; __device__ __forceinline__ unsigned pk2(float lo, float hi) { f32x2_t v = {lo, hi}; bf16x2_t b = __builtin_convertvector(v, bf16x2_t); return __builtin_bit_cast(unsigned, b); }
; #define MFMA32(a, b, c) __builtin_amdgcn_mfma_f32_32x32x16_bf16((a), (b), (c), 0, 0, 0)
; __device__ __forceinline__ void attn_unit(const Frame& F, int layer, int qrow0, int ntiles, int b, int head, float lam, float m2, float lam_init) {
;     ...
;         if (t + 1 < ntiles) AT_QK(na, nb, (t + 1) & 1);
;         float ls = 0.f;
; #pragma unroll
;         for (int i = 0; i < 16; ++i) { sa[i] = __builtin_amdgcn_exp2f(sa[i]); sb[i] = __builtin_amdgcn_exp2f(sb[i]); ls += sa[i] + sb[i]; }
;         lsum += ls;
;         bf16x8 pk[4];
;         { u32x4 w0, w1, w2, w3;
; #pragma unroll
;           for (int i = 0; i < 4; ++i) { w0[i] = pk2(sa[2 * i], sa[2 * i + 1]); w1[i] = pk2(sa[8 + 2 * i], sa[9 + 2 * i]); w2[i] = pk2(sb[2 * i], sb[2 * i + 1]); w3[i] = pk2(sb[8 + 2 * i], sb[9 + 2 * i]); }
;           pk[0] = __builtin_bit_cast(bf16x8, w0); pk[1] = __builtin_bit_cast(bf16x8, w1); pk[2] = __builtin_bit_cast(bf16x8, w2); pk[3] = __builtin_bit_cast(bf16x8, w3); }
;         LAS const unsigned char* Vt = L + AT_V + (t & 1) * AT_VBYTES;
;         __builtin_amdgcn_sched_barrier(0);
;         bf16x8 vfa[4], vfb[4];
; #pragma unroll
;         for (int j = 0; j < 4; ++j) vfa[j] = frag_tr_acc(Vt, AT_VSTR, 0, 32 * j, lane);
; #pragma unroll
;         for (int ks = 0; ks < 4; ks += 2) {
; #pragma unroll
;             for (int j = 0; j < 4; ++j) vfb[j] = frag_tr_acc(Vt, AT_VSTR, 16 * (ks + 1), 32 * j, lane);
; #pragma unroll
;             for (int j = 0; j < 4; ++j) o[j] = MFMA32(pk[ks], vfa[j], o[j]);
;             __builtin_amdgcn_sched_barrier(0);
;             if (ks + 2 < 4) {
; #pragma unroll
;                 for (int j = 0; j < 4; ++j) vfa[j] = frag_tr_acc(Vt, AT_VSTR, 16 * (ks + 2), 32 * j, lane);
;             }
; #pragma unroll
;             for (int j = 0; j < 4; ++j) o[j] = MFMA32(pk[ks + 1], vfb[j], o[j]);
;             __builtin_amdgcn_sched_barrier(0);
;         }
;         if (t + 2 < ntiles) AT_STOREK(t & 1);
;         if (t + 1 < ntiles) AT_STOREV((t + 1) & 1);
.Latt_stage_1:
	ds_write_b128 v179, v[234:237]
	ds_write_b128 v179, v[238:241] offset:8704
	ds_write_b128 v185, v[242:245] offset:34816
	ds_write_b128 v185, v[248:251] offset:45056
	s_add_i32 s5, s2, 2
	s_cmp_ge_u32 s5, 36
	s_cbranch_scc1 .Latt_noqk_1
	ds_read_b128 v[128:131], v190 offset:0
	ds_read_b128 v[132:135], v190 offset:8704
	ds_read_b128 v[136:139], v190 offset:32
	ds_read_b128 v[140:143], v190 offset:8736
	ds_read_b64_tr_b16 v[202:203], v191 offset:34816
	ds_read_b64_tr_b16 v[206:207], v191 offset:34880
	ds_read_b64_tr_b16 v[210:211], v191 offset:34944
	ds_read_b64_tr_b16 v[214:215], v191 offset:35008
	s_waitcnt lgkmcnt(6)
	v_mfma_f32_32x32x16_bf16 v[80:95], v[128:131], v[158:161], v[64:79]
	v_mfma_f32_32x32x16_bf16 v[96:111], v[132:135], v[158:161], v[64:79]
	ds_read_b128 v[128:131], v190 offset:64
	ds_read_b128 v[132:135], v190 offset:8768
	ds_read_b64_tr_b16 v[204:205], v191 offset:37376
	ds_read_b64_tr_b16 v[208:209], v191 offset:37440
	ds_read_b64_tr_b16 v[212:213], v191 offset:37504
	ds_read_b64_tr_b16 v[216:217], v191 offset:37568
	s_waitcnt lgkmcnt(10)
	v_mfma_f32_32x32x16_bf16 v[80:95], v[136:139], v[154:157], v[80:95]
	v_mfma_f32_32x32x16_bf16 v[96:111], v[140:143], v[154:157], v[96:111]
	ds_read_b128 v[136:139], v190 offset:96
	ds_read_b128 v[140:143], v190 offset:8800
	s_waitcnt lgkmcnt(6)
	v_mfma_f32_32x32x16_bf16 v[80:95], v[128:131], v[150:153], v[80:95]
	v_mfma_f32_32x32x16_bf16 v[96:111], v[132:135], v[150:153], v[96:111]
	ds_read_b64_tr_b16 v[218:219], v191 offset:39936
	ds_read_b64_tr_b16 v[222:223], v191 offset:40000
	ds_read_b64_tr_b16 v[226:227], v191 offset:40064
	ds_read_b64_tr_b16 v[230:231], v191 offset:40128
	ds_read_b64_tr_b16 v[220:221], v191 offset:42496
	ds_read_b64_tr_b16 v[224:225], v191 offset:42560
	ds_read_b64_tr_b16 v[228:229], v191 offset:42624
	ds_read_b64_tr_b16 v[232:233], v191 offset:42688
	s_waitcnt lgkmcnt(8)
	v_mfma_f32_32x32x16_bf16 v[80:95], v[136:139], v[146:149], v[80:95]
	v_mfma_f32_32x32x16_bf16 v[96:111], v[140:143], v[146:149], v[96:111]
	s_branch .Latt_pv_1

; #define LAS __attribute__((address_space(3)))
; #define MFMA32(a, b, c) __builtin_amdgcn_mfma_f32_32x32x16_bf16((a), (b), (c), 0, 0, 0)
; #define AT_STOREK(st) do { _Pragma("unroll") for (int i_ = 0; i_ < 2; ++i_) *(LAS u32x4*)(L + AT_K + (st) * AT_KBYTES + (prow0 + 32 * i_) * AT_KSTR + pch * 16) = kreg[i_]; } while (0)
; #define AT_STOREV(st) do { _Pragma("unroll") for (int i_ = 0; i_ < 2; ++i_) *(LAS u32x4*)(L + AT_V + (st) * AT_VBYTES + (prow0 + 32 * i_) * AT_VSTR + pch * 16) = vreg[i_]; } while (0)
; __device__ __forceinline__ void attn_unit(const Frame& F, int layer, int qrow0, int ntiles, int b, int head, float lam, float m2, float lam_init) {
;     ...
;         LAS const unsigned char* Vt = L + AT_V + (t & 1) * AT_VBYTES;
;         __builtin_amdgcn_sched_barrier(0);
;         bf16x8 vfa[4], vfb[4];
; #pragma unroll
;         for (int j = 0; j < 4; ++j) vfa[j] = frag_tr_acc(Vt, AT_VSTR, 0, 32 * j, lane);
; #pragma unroll
;         for (int ks = 0; ks < 4; ks += 2) {
; #pragma unroll
;             for (int j = 0; j < 4; ++j) vfb[j] = frag_tr_acc(Vt, AT_VSTR, 16 * (ks + 1), 32 * j, lane);
; #pragma unroll
;             for (int j = 0; j < 4; ++j) o[j] = MFMA32(pk[ks], vfa[j], o[j]);
;             __builtin_amdgcn_sched_barrier(0);
;             if (ks + 2 < 4) {
; #pragma unroll
;                 for (int j = 0; j < 4; ++j) vfa[j] = frag_tr_acc(Vt, AT_VSTR, 16 * (ks + 2), 32 * j, lane);
;             }
; #pragma unroll
;             for (int j = 0; j < 4; ++j) o[j] = MFMA32(pk[ks + 1], vfb[j], o[j]);
;             __builtin_amdgcn_sched_barrier(0);
;         }
;         if (t + 2 < ntiles) AT_STOREK(t & 1);
;         if (t + 1 < ntiles) AT_STOREV((t + 1) & 1);
;         __syncthreads();
;         sa = na; sb = nb;
;     }
.Latt_pv_1:
	v_mfma_f32_32x32x16_bf16 v[32:47], v[112:115], v[202:205], v[32:47]
	v_mfma_f32_32x32x16_bf16 v[48:63], v[112:115], v[206:209], v[48:63]
	v_mfma_f32_32x32x16_bf16 v[0:15], v[112:115], v[210:213], v[0:15]
	v_mfma_f32_32x32x16_bf16 v[16:31], v[112:115], v[214:217], v[16:31]
	ds_read_b64_tr_b16 v[202:203], v191 offset:45056
	ds_read_b64_tr_b16 v[206:207], v191 offset:45120
	ds_read_b64_tr_b16 v[210:211], v191 offset:45184
	ds_read_b64_tr_b16 v[214:215], v191 offset:45248
	ds_read_b64_tr_b16 v[204:205], v191 offset:47616
	ds_read_b64_tr_b16 v[208:209], v191 offset:47680
	ds_read_b64_tr_b16 v[212:213], v191 offset:47744
	s_waitcnt lgkmcnt(14)
	ds_read_b64_tr_b16 v[216:217], v191 offset:47808
	s_waitcnt lgkmcnt(8)
	v_mfma_f32_32x32x16_bf16 v[32:47], v[116:119], v[218:221], v[32:47]
	v_mfma_f32_32x32x16_bf16 v[48:63], v[116:119], v[222:225], v[48:63]
	v_mfma_f32_32x32x16_bf16 v[0:15], v[116:119], v[226:229], v[0:15]
	v_mfma_f32_32x32x16_bf16 v[16:31], v[116:119], v[230:233], v[16:31]
	ds_read_b64_tr_b16 v[218:219], v191 offset:50176
	ds_read_b64_tr_b16 v[222:223], v191 offset:50240
	ds_read_b64_tr_b16 v[226:227], v191 offset:50304
	ds_read_b64_tr_b16 v[230:231], v191 offset:50368
	ds_read_b64_tr_b16 v[220:221], v191 offset:52736
	ds_read_b64_tr_b16 v[224:225], v191 offset:52800
	ds_read_b64_tr_b16 v[228:229], v191 offset:52864
	s_waitcnt lgkmcnt(14)
	ds_read_b64_tr_b16 v[232:233], v191 offset:52928
	s_waitcnt lgkmcnt(8)
	v_mfma_f32_32x32x16_bf16 v[32:47], v[120:123], v[202:205], v[32:47]
	v_mfma_f32_32x32x16_bf16 v[48:63], v[120:123], v[206:209], v[48:63]
	v_mfma_f32_32x32x16_bf16 v[0:15], v[120:123], v[210:213], v[0:15]
	v_mfma_f32_32x32x16_bf16 v[16:31], v[120:123], v[214:217], v[16:31]
	s_waitcnt lgkmcnt(0)
	v_mfma_f32_32x32x16_bf16 v[32:47], v[124:127], v[218:221], v[32:47]
	v_mfma_f32_32x32x16_bf16 v[48:63], v[124:127], v[222:225], v[48:63]
	v_mfma_f32_32x32x16_bf16 v[0:15], v[124:127], v[226:229], v[0:15]
	v_mfma_f32_32x32x16_bf16 v[16:31], v[124:127], v[230:233], v[16:31]
	s_barrier
	s_add_i32 s2, s2, 2
	s_cmp_lt_u32 s2, 36
	s_cbranch_scc1 .Latt_loop
	s_cmp_ge_u32 s12, 4
	s_cbranch_scc1 .Latt_trail1
	s_barrier
